# v17 + dilated attention stagger of waves 4-7 by ~5k cycles
# baseline (speedup 1.0000x reference)
.LBB0_286:
	s_or_b64 exec, exec, s[4:5]
	s_ashr_i32 s5, s7, 9
	s_and_b32 s24, s5, -2
	s_ashr_i32 s75, s7, 6
	s_lshr_b32 s5, 16, s24
	s_and_b32 s74, s6, 3
	s_ashr_i32 s4, s3, 3
	s_and_b32 s3, s75, 15
	s_sub_i32 s6, 4, s24
	s_add_i32 s5, s5, -1
	s_lshr_b32 s25, s3, s6
	s_and_b32 s3, s5, s3
	s_ashr_i32 s5, s4, 31
	s_lshl_b64 s[20:21], s[4:5], 12
	s_lshr_b32 s6, 0x400, s24
	s_or_b32 s4, s20, s25
	s_mul_i32 s6, s6, s74
	s_lshl_b32 s3, s3, 6
	s_mul_hi_u32 s26, s4, 0x1800
	s_mul_i32 s76, s21, 0x1800
	s_add_i32 s3, s3, s6
	s_lshl_b64 s[22:23], 8, s24
	s_mul_i32 s25, s4, 0x1800
	s_add_i32 s26, s26, s76
	s_add_u32 s25, s10, s25
	s_addc_u32 s26, s11, s26
	s_lshl_b32 s27, s16, 6
	s_lshl_b32 s16, s16, 7
	s_add_u32 s25, s25, s16
	v_sub_co_u32_e64 v2, s[6:7], s3, 64
	s_addc_u32 s26, s26, 0
	s_and_b64 s[6:7], s[6:7], exec
	v_readfirstlane_b32 s6, v2
	s_cselect_b32 s6, s3, s6
	s_ashr_i32 s7, s6, 31
	s_lshl_b64 s[6:7], s[6:7], s24
	v_bfe_u32 v3, v0, 3, 3
	s_mulk_i32 s7, 0x1800
	s_mul_hi_u32 s28, s6, 0x1800
	v_lshlrev_b32_e32 v3, s24, v3
	s_add_i32 s28, s28, s7
	s_mulk_i32 s6, 0x1800
	v_mul_lo_u32 v3, v3, s49
	v_lshlrev_b32_e32 v180, 3, v0
	s_add_u32 s6, s25, s6
	v_and_or_b32 v168, v180, 56, v3
	s_addc_u32 s7, s26, s28
	v_lshl_add_u64 v[2:3], v[168:169], 1, s[6:7]
	v_lshl_add_u64 v[4:5], v[2:3], 0, s[18:19]
	v_mad_u64_u32 v[6:7], s[6:7], s22, v172, v[4:5]
	s_mul_i32 s6, s23, 0x1800
	s_nop 0
	v_add_u32_e32 v7, s6, v7
	v_mad_u64_u32 v[8:9], s[6:7], s22, v173, v[4:5]
	s_mul_i32 s6, s23, 0x3000
	s_waitcnt lgkmcnt(0)
	s_barrier
	v_add_u32_e32 v9, s6, v9
	global_load_dwordx4 v[128:131], v[6:7], off
	global_load_dwordx4 v[132:135], v[8:9], off
	v_mad_u64_u32 v[6:7], s[6:7], s22, v174, v[4:5]
	s_mul_i32 s6, s23, 0x4800
	s_nop 0
	v_add_u32_e32 v7, s6, v7
	v_mad_u64_u32 v[8:9], s[6:7], s22, v175, v[4:5]
	s_mul_i32 s6, s23, 0x6000
	s_nop 0
	v_add_u32_e32 v9, s6, v9
	global_load_dwordx4 v[136:139], v[6:7], off
	global_load_dwordx4 v[140:143], v[8:9], off
	v_mad_u64_u32 v[6:7], s[6:7], s22, v176, v[4:5]
	s_mul_i32 s6, s23, 0x7800
	v_and_b32_e32 v1, 31, v0
	v_add_u32_e32 v7, s6, v7
	v_mad_u64_u32 v[8:9], s[6:7], s22, v177, v[4:5]
	s_mul_i32 s6, s23, 0x9000
	v_add_u32_e32 v168, s3, v1
	s_mov_b32 s5, s21
	v_add_u32_e32 v9, s6, v9
	global_load_dwordx4 v[144:147], v[6:7], off
	global_load_dwordx4 v[152:155], v[8:9], off
	v_mad_u64_u32 v[4:5], s[6:7], s22, v178, v[4:5]
	v_lshlrev_b64 v[6:7], s24, v[168:169]
	s_mul_i32 s6, s23, 0xa800
	v_lshl_add_u64 v[6:7], v[6:7], 0, s[4:5]
	v_add_u32_e32 v5, s6, v5
	v_mad_u64_u32 v[8:9], s[6:7], v6, s56, v[170:171]
	v_mov_b32_e32 v6, v9
	v_mad_u64_u32 v[6:7], s[6:7], v7, s56, v[6:7]
	v_add_co_u32_e32 v2, vcc, s57, v2
	v_mov_b32_e32 v9, v6
	v_lshrrev_b32_e32 v1, 1, v0
	v_addc_co_u32_e32 v3, vcc, 0, v3, vcc
	v_lshl_add_u64 v[6:7], v[8:9], 0, s[16:17]
	v_and_b32_e32 v8, 16, v1
	v_mov_b32_e32 v9, v169
	v_add_u32_e32 v168, 32, v168
	v_lshl_add_u64 v[6:7], v[6:7], 0, v[8:9]
	global_load_dwordx4 v[148:151], v[2:3], off
	global_load_dwordx4 v[96:99], v[6:7], off offset:3072
	global_load_dwordx4 v[100:103], v[6:7], off offset:3104
	global_load_dwordx4 v[104:107], v[6:7], off offset:3136
	v_lshlrev_b64 v[2:3], s24, v[168:169]
	v_lshl_add_u64 v[2:3], v[2:3], 0, s[4:5]
	v_mad_u64_u32 v[10:11], s[4:5], v2, s56, v[170:171]
	v_mov_b32_e32 v2, v11
	v_mad_u64_u32 v[2:3], s[4:5], v3, s56, v[2:3]
	v_mov_b32_e32 v11, v2
	v_lshl_add_u64 v[2:3], v[10:11], 0, s[16:17]
	v_lshl_add_u64 v[2:3], v[2:3], 0, v[8:9]
	global_load_dwordx4 v[108:111], v[6:7], off offset:3168
	global_load_dwordx4 v[112:115], v[2:3], off offset:3072
	global_load_dwordx4 v[116:119], v[2:3], off offset:3104
	global_load_dwordx4 v[120:123], v[2:3], off offset:3136
	global_load_dwordx4 v[156:159], v[4:5], off
	global_load_dwordx4 v[124:127], v[2:3], off offset:3168
	s_lshl_b32 s3, s75, 8
	s_lshl_b32 s4, s75, 13
	s_add_i32 s79, s4, 0
	s_add_i32 s81, s3, 0
	s_add_i32 s80, s79, 0x10000
	s_add_i32 s81, s81, 0x21000
	s_add_u32 s22, s10, s16
	v_and_b32_e32 v181, 63, v0
	s_mov_b32 s78, 0
	s_addc_u32 s23, s11, 0
	s_lshl_b32 s77, s27, 1
	s_cmp_lt_u32 s75, 4
	s_cbranch_scc1 .Ldil_nostag
	s_sleep 80
